# baseline (speedup 1.0000x reference)
.Lpc_anchor:
	s_add_u32 s44, s44, _Z7dog_finPKfS0_Pf-.Lpc_anchor
	s_addc_u32 s45, s45, 0
	s_load_dwordx16 s[48:63], s[44:45], 0x0
	s_load_dwordx16 s[64:79], s[44:45], 0x40
	s_load_dwordx16 s[80:95], s[44:45], 0x80
	v_mul_f32_e32 v16, v12, v12
	v_add_f32_e32 v17, 0x3f800000, v12
	v_add_f32_e32 v18, 0x40000000, v12
	v_add_f32_e32 v19, 0x40400000, v12
	v_mul_f32_e32 v17, v17, v17
	v_mul_f32_e32 v18, v18, v18
	v_mul_f32_e32 v19, v19, v19
	v_mul_f32_e32 v20, v8, v16
	v_mul_f32_e32 v24, v9, v16
	v_mul_f32_e32 v21, v8, v17
	v_mul_f32_e32 v25, v9, v17
	v_mul_f32_e32 v22, v8, v18
	v_mul_f32_e32 v26, v9, v18
	v_mul_f32_e32 v23, v8, v19
	v_mul_f32_e32 v27, v9, v19
	v_exp_f32_e32 v20, v20
	v_exp_f32_e32 v21, v21
	v_exp_f32_e32 v22, v22
	v_exp_f32_e32 v23, v23
	v_exp_f32_e32 v24, v24
	v_exp_f32_e32 v25, v25
	v_exp_f32_e32 v26, v26
	v_exp_f32_e32 v27, v27
	v_cvt_pk_f16_f32 v32, v20, v21
	v_cvt_pk_f16_f32 v33, v22, v23
	v_cvt_pk_f16_f32 v64, v24, v25
	v_cvt_pk_f16_f32 v65, v26, v27
	v_add_f32_e32 v16, 0x40800000, v12
	v_add_f32_e32 v17, 0x40a00000, v12
	v_add_f32_e32 v18, 0x40c00000, v12
	v_add_f32_e32 v19, 0x40e00000, v12
	v_mul_f32_e32 v16, v16, v16
	v_mul_f32_e32 v17, v17, v17
	v_mul_f32_e32 v18, v18, v18
	v_mul_f32_e32 v19, v19, v19
	v_mul_f32_e32 v20, v8, v16
	v_mul_f32_e32 v24, v9, v16
	v_mul_f32_e32 v21, v8, v17
	v_mul_f32_e32 v25, v9, v17
	v_mul_f32_e32 v22, v8, v18
	v_mul_f32_e32 v26, v9, v18
	v_mul_f32_e32 v23, v8, v19
	v_mul_f32_e32 v27, v9, v19
	v_exp_f32_e32 v20, v20
	v_exp_f32_e32 v21, v21
	v_exp_f32_e32 v22, v22
	v_exp_f32_e32 v23, v23
	v_exp_f32_e32 v24, v24
	v_exp_f32_e32 v25, v25
	v_exp_f32_e32 v26, v26
	v_exp_f32_e32 v27, v27
	v_cvt_pk_f16_f32 v34, v20, v21
	v_cvt_pk_f16_f32 v35, v22, v23
	v_cvt_pk_f16_f32 v66, v24, v25
	v_cvt_pk_f16_f32 v67, v26, v27
	v_add_f32_e32 v16, 0x42000000, v12
	v_add_f32_e32 v17, 0x42040000, v12
	v_add_f32_e32 v18, 0x42080000, v12
	v_add_f32_e32 v19, 0x420c0000, v12
	v_mul_f32_e32 v16, v16, v16
	v_mul_f32_e32 v17, v17, v17
	v_mul_f32_e32 v18, v18, v18
	v_mul_f32_e32 v19, v19, v19
	v_mul_f32_e32 v20, v8, v16
	v_mul_f32_e32 v24, v9, v16
	v_mul_f32_e32 v21, v8, v17
	v_mul_f32_e32 v25, v9, v17
	v_mul_f32_e32 v22, v8, v18
	v_mul_f32_e32 v26, v9, v18
	v_mul_f32_e32 v23, v8, v19
	v_mul_f32_e32 v27, v9, v19
	v_exp_f32_e32 v20, v20
	v_exp_f32_e32 v21, v21
	v_exp_f32_e32 v22, v22
	v_exp_f32_e32 v23, v23
	v_exp_f32_e32 v24, v24
	v_exp_f32_e32 v25, v25
	v_exp_f32_e32 v26, v26
	v_exp_f32_e32 v27, v27
	v_cvt_pk_f16_f32 v36, v20, v21
	v_cvt_pk_f16_f32 v37, v22, v23
	v_cvt_pk_f16_f32 v68, v24, v25
	v_cvt_pk_f16_f32 v69, v26, v27
	v_add_f32_e32 v16, 0x42100000, v12
	v_add_f32_e32 v17, 0x42140000, v12
	v_add_f32_e32 v18, 0x42180000, v12
	v_add_f32_e32 v19, 0x421c0000, v12
	v_mul_f32_e32 v16, v16, v16
	v_mul_f32_e32 v17, v17, v17
	v_mul_f32_e32 v18, v18, v18
	v_mul_f32_e32 v19, v19, v19
	v_mul_f32_e32 v20, v8, v16
	v_mul_f32_e32 v24, v9, v16
	v_mul_f32_e32 v21, v8, v17
	v_mul_f32_e32 v25, v9, v17
	v_mul_f32_e32 v22, v8, v18
	v_mul_f32_e32 v26, v9, v18
	v_mul_f32_e32 v23, v8, v19
	v_mul_f32_e32 v27, v9, v19
	v_exp_f32_e32 v20, v20
	v_exp_f32_e32 v21, v21
	v_exp_f32_e32 v22, v22
	v_exp_f32_e32 v23, v23
	v_exp_f32_e32 v24, v24
	v_exp_f32_e32 v25, v25
	v_exp_f32_e32 v26, v26
	v_exp_f32_e32 v27, v27
	v_cvt_pk_f16_f32 v38, v20, v21
	v_cvt_pk_f16_f32 v39, v22, v23
	v_cvt_pk_f16_f32 v70, v24, v25
	v_cvt_pk_f16_f32 v71, v26, v27
	v_add_u32_e32 v6, 0x8000, v6
	global_load_dwordx4 v[160:163], v6, s[12:13] offset:0 nt
	global_load_dwordx4 v[164:167], v6, s[12:13] offset:1024 nt
	global_load_dwordx4 v[168:171], v6, s[12:13] offset:2048 nt
	global_load_dwordx4 v[172:175], v6, s[12:13] offset:3072 nt
	v_add_f32_e32 v16, 0x42800000, v12
	v_add_f32_e32 v17, 0x42820000, v12
	v_add_f32_e32 v18, 0x42840000, v12
	v_add_f32_e32 v19, 0x42860000, v12
	v_mul_f32_e32 v16, v16, v16
	v_mul_f32_e32 v17, v17, v17
	v_mul_f32_e32 v18, v18, v18
	v_mul_f32_e32 v19, v19, v19
	v_mul_f32_e32 v20, v8, v16
	v_mul_f32_e32 v24, v9, v16
	v_mul_f32_e32 v21, v8, v17
	v_mul_f32_e32 v25, v9, v17
	v_mul_f32_e32 v22, v8, v18
	v_mul_f32_e32 v26, v9, v18
	v_mul_f32_e32 v23, v8, v19
	v_mul_f32_e32 v27, v9, v19
	v_exp_f32_e32 v20, v20
	v_exp_f32_e32 v21, v21
	v_exp_f32_e32 v22, v22
	v_exp_f32_e32 v23, v23
	v_exp_f32_e32 v24, v24
	v_exp_f32_e32 v25, v25
	v_exp_f32_e32 v26, v26
	v_exp_f32_e32 v27, v27
	v_cvt_pk_f16_f32 v40, v20, v21
	v_cvt_pk_f16_f32 v41, v22, v23
	v_cvt_pk_f16_f32 v72, v24, v25
	v_cvt_pk_f16_f32 v73, v26, v27
	v_add_f32_e32 v16, 0x42880000, v12
	v_add_f32_e32 v17, 0x428a0000, v12
	v_add_f32_e32 v18, 0x428c0000, v12
	v_add_f32_e32 v19, 0x428e0000, v12
	v_mul_f32_e32 v16, v16, v16
	v_mul_f32_e32 v17, v17, v17
	v_mul_f32_e32 v18, v18, v18
	v_mul_f32_e32 v19, v19, v19
	v_mul_f32_e32 v20, v8, v16
	v_mul_f32_e32 v24, v9, v16
	v_mul_f32_e32 v21, v8, v17
	v_mul_f32_e32 v25, v9, v17
	v_mul_f32_e32 v22, v8, v18
	v_mul_f32_e32 v26, v9, v18
	v_mul_f32_e32 v23, v8, v19
	v_mul_f32_e32 v27, v9, v19
	v_exp_f32_e32 v20, v20
	v_exp_f32_e32 v21, v21
	v_exp_f32_e32 v22, v22
	v_exp_f32_e32 v23, v23
	v_exp_f32_e32 v24, v24
	v_exp_f32_e32 v25, v25
	v_exp_f32_e32 v26, v26
	v_exp_f32_e32 v27, v27
	v_cvt_pk_f16_f32 v42, v20, v21
	v_cvt_pk_f16_f32 v43, v22, v23
	v_cvt_pk_f16_f32 v74, v24, v25
	v_cvt_pk_f16_f32 v75, v26, v27
	v_add_f32_e32 v16, 0x42c00000, v12
	v_add_f32_e32 v17, 0x42c20000, v12
	v_add_f32_e32 v18, 0x42c40000, v12
	v_add_f32_e32 v19, 0x42c60000, v12
	v_mul_f32_e32 v16, v16, v16
	v_mul_f32_e32 v17, v17, v17
	v_mul_f32_e32 v18, v18, v18
	v_mul_f32_e32 v19, v19, v19
	v_mul_f32_e32 v20, v8, v16
	v_mul_f32_e32 v24, v9, v16
	v_mul_f32_e32 v21, v8, v17
	v_mul_f32_e32 v25, v9, v17
	v_mul_f32_e32 v22, v8, v18
	v_mul_f32_e32 v26, v9, v18
	v_mul_f32_e32 v23, v8, v19
	v_mul_f32_e32 v27, v9, v19
	v_exp_f32_e32 v20, v20
	v_exp_f32_e32 v21, v21
	v_exp_f32_e32 v22, v22
	v_exp_f32_e32 v23, v23
	v_exp_f32_e32 v24, v24
	v_exp_f32_e32 v25, v25
	v_exp_f32_e32 v26, v26
	v_exp_f32_e32 v27, v27
	v_cvt_pk_f16_f32 v44, v20, v21
	v_cvt_pk_f16_f32 v45, v22, v23
	v_cvt_pk_f16_f32 v76, v24, v25
	v_cvt_pk_f16_f32 v77, v26, v27
	v_add_f32_e32 v16, 0x42c80000, v12
	v_add_f32_e32 v17, 0x42ca0000, v12
	v_add_f32_e32 v18, 0x42cc0000, v12
	v_add_f32_e32 v19, 0x42ce0000, v12
	v_mul_f32_e32 v16, v16, v16
	v_mul_f32_e32 v17, v17, v17
	v_mul_f32_e32 v18, v18, v18
	v_mul_f32_e32 v19, v19, v19
	v_mul_f32_e32 v20, v8, v16
	v_mul_f32_e32 v24, v9, v16
	v_mul_f32_e32 v21, v8, v17
	v_mul_f32_e32 v25, v9, v17
	v_mul_f32_e32 v22, v8, v18
	v_mul_f32_e32 v26, v9, v18
	v_mul_f32_e32 v23, v8, v19
	v_mul_f32_e32 v27, v9, v19
	v_exp_f32_e32 v20, v20
	v_exp_f32_e32 v21, v21
	v_exp_f32_e32 v22, v22
	v_exp_f32_e32 v23, v23
	v_exp_f32_e32 v24, v24
	v_exp_f32_e32 v25, v25
	v_exp_f32_e32 v26, v26
	v_exp_f32_e32 v27, v27
	v_cvt_pk_f16_f32 v46, v20, v21
	v_cvt_pk_f16_f32 v47, v22, v23
	v_cvt_pk_f16_f32 v78, v24, v25
	v_cvt_pk_f16_f32 v79, v26, v27
	v_add_u32_e32 v6, 0x8000, v6
	global_load_dwordx4 v[176:179], v6, s[12:13] offset:0 nt
	global_load_dwordx4 v[180:183], v6, s[12:13] offset:1024 nt
	global_load_dwordx4 v[184:187], v6, s[12:13] offset:2048 nt
	global_load_dwordx4 v[188:191], v6, s[12:13] offset:3072 nt
	s_mov_b32 s29, 0
	v_mov_b32_e32 v224, 0
	v_mov_b32_e32 v225, 0
	v_mov_b32_e32 v226, 0
	v_mov_b32_e32 v227, 0
	s_lshl_b32 s6, s6, 6
	s_add_i32 s6, s6, s7
	s_lshl_b32 s6, s6, 10
	v_add_u32_e32 v5, s6, v5
.Lblk0:
	s_cmp_eq_u32 s29, 0
	s_cbranch_scc1 .Lblk0_first
	s_waitcnt vmcnt(12)
	s_branch .Lblk0_go
.Lblk0_first:
	s_waitcnt vmcnt(12)
.Lblk0_go:
	v_add_f32_e32 v128, v128, v129
	v_add_f32_e32 v130, v130, v131
	v_add_f32_e32 v132, v132, v133
	v_add_f32_e32 v134, v134, v135
	v_add_f32_e32 v136, v136, v137
	v_add_f32_e32 v138, v138, v139
	v_add_f32_e32 v140, v140, v141
	v_add_f32_e32 v142, v142, v143
	v_add_f32_e32 v128, v128, v130
	v_add_f32_e32 v132, v132, v134
	v_add_f32_e32 v136, v136, v138
	v_add_f32_e32 v140, v140, v142
	v_cndmask_b32_e64 v130, v128, v132, s[30:31]
	v_cndmask_b32_e64 v134, v136, v140, s[30:31]
	v_cndmask_b32_e64 v129, v132, v128, s[30:31]
	v_cndmask_b32_e64 v133, v140, v136, s[30:31]
	v_add_f32_dpp v129, v130, v129 quad_perm:[1,0,3,2] row_mask:0xf bank_mask:0xf bound_ctrl:1
	v_add_f32_dpp v133, v134, v133 quad_perm:[1,0,3,2] row_mask:0xf bank_mask:0xf bound_ctrl:1
	v_cndmask_b32_e64 v135, v129, v133, s[32:33]
	v_cndmask_b32_e64 v131, v133, v129, s[32:33]
	s_nop 1
	v_add_f32_dpp v131, v135, v131 quad_perm:[2,3,0,1] row_mask:0xf bank_mask:0xf bound_ctrl:1
	v_cvt_f16_f32_e32 v131, v131
	ds_write_b16 v14, v131 offset:0
	s_cmp_eq_u32 s29, 0
	s_cbranch_scc0 .Lblk0_done
	v_add_u32_e32 v6, 0x8000, v6
	global_load_dwordx4 v[128:131], v6, s[12:13] offset:0 nt
	global_load_dwordx4 v[132:135], v6, s[12:13] offset:1024 nt
	global_load_dwordx4 v[136:139], v6, s[12:13] offset:2048 nt
	global_load_dwordx4 v[140:143], v6, s[12:13] offset:3072 nt
	v_mul_f32_e32 v16, v2, v2
	v_add_f32_e32 v17, 0x3f800000, v2
	v_add_f32_e32 v18, 0x40000000, v2
	v_add_f32_e32 v19, 0x40400000, v2
	v_mul_f32_e32 v17, v17, v17
	v_mul_f32_e32 v18, v18, v18
	v_mul_f32_e32 v19, v19, v19
	v_mul_f32_e32 v20, v28, v16
	v_mul_f32_e32 v24, v29, v16
	v_mul_f32_e32 v21, v28, v17
	v_mul_f32_e32 v25, v29, v17
	v_mul_f32_e32 v22, v28, v18
	v_mul_f32_e32 v26, v29, v18
	v_mul_f32_e32 v23, v28, v19
	v_mul_f32_e32 v27, v29, v19
	v_exp_f32_e32 v20, v20
	v_exp_f32_e32 v21, v21
	v_exp_f32_e32 v22, v22
	v_exp_f32_e32 v23, v23
	v_exp_f32_e32 v24, v24
	v_exp_f32_e32 v25, v25
	v_exp_f32_e32 v26, v26
	v_exp_f32_e32 v27, v27
	v_cvt_pk_f16_f32 v48, v20, v21
	v_cvt_pk_f16_f32 v49, v22, v23
	v_cvt_pk_f16_f32 v80, v24, v25
	v_cvt_pk_f16_f32 v81, v26, v27
	v_add_f32_e32 v16, 0x40800000, v2
	v_add_f32_e32 v17, 0x40a00000, v2
	v_add_f32_e32 v18, 0x40c00000, v2
	v_add_f32_e32 v19, 0x40e00000, v2
	v_mul_f32_e32 v16, v16, v16
	v_mul_f32_e32 v17, v17, v17
	v_mul_f32_e32 v18, v18, v18
	v_mul_f32_e32 v19, v19, v19
	v_mul_f32_e32 v20, v28, v16
	v_mul_f32_e32 v24, v29, v16
	v_mul_f32_e32 v21, v28, v17
	v_mul_f32_e32 v25, v29, v17
	v_mul_f32_e32 v22, v28, v18
	v_mul_f32_e32 v26, v29, v18
	v_mul_f32_e32 v23, v28, v19
	v_mul_f32_e32 v27, v29, v19
	v_exp_f32_e32 v20, v20
	v_exp_f32_e32 v21, v21
	v_exp_f32_e32 v22, v22
	v_exp_f32_e32 v23, v23
	v_exp_f32_e32 v24, v24
	v_exp_f32_e32 v25, v25
	v_exp_f32_e32 v26, v26
	v_exp_f32_e32 v27, v27
	v_cvt_pk_f16_f32 v50, v20, v21
	v_cvt_pk_f16_f32 v51, v22, v23
	v_cvt_pk_f16_f32 v82, v24, v25
	v_cvt_pk_f16_f32 v83, v26, v27
	v_add_f32_e32 v16, 0x42000000, v2
	v_add_f32_e32 v17, 0x42040000, v2
	v_add_f32_e32 v18, 0x42080000, v2
	v_add_f32_e32 v19, 0x420c0000, v2
	v_mul_f32_e32 v16, v16, v16
	v_mul_f32_e32 v17, v17, v17
	v_mul_f32_e32 v18, v18, v18
	v_mul_f32_e32 v19, v19, v19
	v_mul_f32_e32 v20, v28, v16
	v_mul_f32_e32 v24, v29, v16
	v_mul_f32_e32 v21, v28, v17
	v_mul_f32_e32 v25, v29, v17
	v_mul_f32_e32 v22, v28, v18
	v_mul_f32_e32 v26, v29, v18
	v_mul_f32_e32 v23, v28, v19
	v_mul_f32_e32 v27, v29, v19
	v_exp_f32_e32 v20, v20
	v_exp_f32_e32 v21, v21
	v_exp_f32_e32 v22, v22
	v_exp_f32_e32 v23, v23
	v_exp_f32_e32 v24, v24
	v_exp_f32_e32 v25, v25
	v_exp_f32_e32 v26, v26
	v_exp_f32_e32 v27, v27
	v_cvt_pk_f16_f32 v52, v20, v21
	v_cvt_pk_f16_f32 v53, v22, v23
	v_cvt_pk_f16_f32 v84, v24, v25
	v_cvt_pk_f16_f32 v85, v26, v27
	v_add_f32_e32 v16, 0x42100000, v2
	v_add_f32_e32 v17, 0x42140000, v2
	v_add_f32_e32 v18, 0x42180000, v2
	v_add_f32_e32 v19, 0x421c0000, v2
	v_mul_f32_e32 v16, v16, v16
	v_mul_f32_e32 v17, v17, v17
	v_mul_f32_e32 v18, v18, v18
	v_mul_f32_e32 v19, v19, v19
	v_mul_f32_e32 v20, v28, v16
	v_mul_f32_e32 v24, v29, v16
	v_mul_f32_e32 v21, v28, v17
	v_mul_f32_e32 v25, v29, v17
	v_mul_f32_e32 v22, v28, v18
	v_mul_f32_e32 v26, v29, v18
	v_mul_f32_e32 v23, v28, v19
	v_mul_f32_e32 v27, v29, v19
	v_exp_f32_e32 v20, v20
	v_exp_f32_e32 v21, v21
	v_exp_f32_e32 v22, v22
	v_exp_f32_e32 v23, v23
	v_exp_f32_e32 v24, v24
	v_exp_f32_e32 v25, v25
	v_exp_f32_e32 v26, v26
	v_exp_f32_e32 v27, v27
	v_cvt_pk_f16_f32 v54, v20, v21
	v_cvt_pk_f16_f32 v55, v22, v23
	v_cvt_pk_f16_f32 v86, v24, v25
	v_cvt_pk_f16_f32 v87, v26, v27
.Lblk0_done:
.Lblk1:
	s_cmp_eq_u32 s29, 0
	s_cbranch_scc1 .Lblk1_first
	s_waitcnt vmcnt(8)
	s_branch .Lblk1_go

.Lblk1_go:
	v_add_f32_e32 v144, v144, v145
	v_add_f32_e32 v146, v146, v147
	v_add_f32_e32 v148, v148, v149
	v_add_f32_e32 v150, v150, v151
	v_add_f32_e32 v152, v152, v153
	v_add_f32_e32 v154, v154, v155
	v_add_f32_e32 v156, v156, v157
	v_add_f32_e32 v158, v158, v159
	v_add_f32_e32 v144, v144, v146
	v_add_f32_e32 v148, v148, v150
	v_add_f32_e32 v152, v152, v154
	v_add_f32_e32 v156, v156, v158
	v_cndmask_b32_e64 v146, v144, v148, s[30:31]
	v_cndmask_b32_e64 v150, v152, v156, s[30:31]
	v_cndmask_b32_e64 v145, v148, v144, s[30:31]
	v_cndmask_b32_e64 v149, v156, v152, s[30:31]
	v_add_f32_dpp v145, v146, v145 quad_perm:[1,0,3,2] row_mask:0xf bank_mask:0xf bound_ctrl:1
	v_add_f32_dpp v149, v150, v149 quad_perm:[1,0,3,2] row_mask:0xf bank_mask:0xf bound_ctrl:1
	v_cndmask_b32_e64 v151, v145, v149, s[32:33]
	v_cndmask_b32_e64 v147, v149, v145, s[32:33]
	s_nop 1
	v_add_f32_dpp v147, v151, v147 quad_perm:[2,3,0,1] row_mask:0xf bank_mask:0xf bound_ctrl:1
	v_cvt_f16_f32_e32 v147, v147
	ds_write_b16 v14, v147 offset:1088
	s_cmp_eq_u32 s29, 0
	s_cbranch_scc0 .Lblk1_done
	v_add_u32_e32 v6, 0x8000, v6
	global_load_dwordx4 v[144:147], v6, s[12:13] offset:0 nt
	global_load_dwordx4 v[148:151], v6, s[12:13] offset:1024 nt
	global_load_dwordx4 v[152:155], v6, s[12:13] offset:2048 nt
	global_load_dwordx4 v[156:159], v6, s[12:13] offset:3072 nt
	v_add_f32_e32 v16, 0x42800000, v2
	v_add_f32_e32 v17, 0x42820000, v2
	v_add_f32_e32 v18, 0x42840000, v2
	v_add_f32_e32 v19, 0x42860000, v2
	v_mul_f32_e32 v16, v16, v16
	v_mul_f32_e32 v17, v17, v17
	v_mul_f32_e32 v18, v18, v18
	v_mul_f32_e32 v19, v19, v19
	v_mul_f32_e32 v20, v28, v16
	v_mul_f32_e32 v24, v29, v16
	v_mul_f32_e32 v21, v28, v17
	v_mul_f32_e32 v25, v29, v17
	v_mul_f32_e32 v22, v28, v18
	v_mul_f32_e32 v26, v29, v18
	v_mul_f32_e32 v23, v28, v19
	v_mul_f32_e32 v27, v29, v19
	v_exp_f32_e32 v20, v20
	v_exp_f32_e32 v21, v21
	v_exp_f32_e32 v22, v22
	v_exp_f32_e32 v23, v23
	v_exp_f32_e32 v24, v24
	v_exp_f32_e32 v25, v25
	v_exp_f32_e32 v26, v26
	v_exp_f32_e32 v27, v27
	v_cvt_pk_f16_f32 v56, v20, v21
	v_cvt_pk_f16_f32 v57, v22, v23
	v_cvt_pk_f16_f32 v88, v24, v25
	v_cvt_pk_f16_f32 v89, v26, v27
	v_add_f32_e32 v16, 0x42880000, v2
	v_add_f32_e32 v17, 0x428a0000, v2
	v_add_f32_e32 v18, 0x428c0000, v2
	v_add_f32_e32 v19, 0x428e0000, v2
	v_mul_f32_e32 v16, v16, v16
	v_mul_f32_e32 v17, v17, v17
	v_mul_f32_e32 v18, v18, v18
	v_mul_f32_e32 v19, v19, v19
	v_mul_f32_e32 v20, v28, v16
	v_mul_f32_e32 v24, v29, v16
	v_mul_f32_e32 v21, v28, v17
	v_mul_f32_e32 v25, v29, v17
	v_mul_f32_e32 v22, v28, v18
	v_mul_f32_e32 v26, v29, v18
	v_mul_f32_e32 v23, v28, v19
	v_mul_f32_e32 v27, v29, v19
	v_exp_f32_e32 v20, v20
	v_exp_f32_e32 v21, v21
	v_exp_f32_e32 v22, v22
	v_exp_f32_e32 v23, v23
	v_exp_f32_e32 v24, v24
	v_exp_f32_e32 v25, v25
	v_exp_f32_e32 v26, v26
	v_exp_f32_e32 v27, v27
	v_cvt_pk_f16_f32 v58, v20, v21
	v_cvt_pk_f16_f32 v59, v22, v23
	v_cvt_pk_f16_f32 v90, v24, v25
	v_cvt_pk_f16_f32 v91, v26, v27
	v_add_f32_e32 v16, 0x42c00000, v2
	v_add_f32_e32 v17, 0x42c20000, v2
	v_add_f32_e32 v18, 0x42c40000, v2
	v_add_f32_e32 v19, 0x42c60000, v2
	v_mul_f32_e32 v16, v16, v16
	v_mul_f32_e32 v17, v17, v17
	v_mul_f32_e32 v18, v18, v18
	v_mul_f32_e32 v19, v19, v19
	v_mul_f32_e32 v20, v28, v16
	v_mul_f32_e32 v24, v29, v16
	v_mul_f32_e32 v21, v28, v17
	v_mul_f32_e32 v25, v29, v17
	v_mul_f32_e32 v22, v28, v18
	v_mul_f32_e32 v26, v29, v18
	v_mul_f32_e32 v23, v28, v19
	v_mul_f32_e32 v27, v29, v19
	v_exp_f32_e32 v20, v20
	v_exp_f32_e32 v21, v21
	v_exp_f32_e32 v22, v22
	v_exp_f32_e32 v23, v23
	v_exp_f32_e32 v24, v24
	v_exp_f32_e32 v25, v25
	v_exp_f32_e32 v26, v26
	v_exp_f32_e32 v27, v27
	v_cvt_pk_f16_f32 v60, v20, v21
	v_cvt_pk_f16_f32 v61, v22, v23
	v_cvt_pk_f16_f32 v92, v24, v25
	v_cvt_pk_f16_f32 v93, v26, v27
	v_add_f32_e32 v16, 0x42c80000, v2
	v_add_f32_e32 v17, 0x42ca0000, v2
	v_add_f32_e32 v18, 0x42cc0000, v2
	v_add_f32_e32 v19, 0x42ce0000, v2
	v_mul_f32_e32 v16, v16, v16
	v_mul_f32_e32 v17, v17, v17
	v_mul_f32_e32 v18, v18, v18
	v_mul_f32_e32 v19, v19, v19
	v_mul_f32_e32 v20, v28, v16
	v_mul_f32_e32 v24, v29, v16
	v_mul_f32_e32 v21, v28, v17
	v_mul_f32_e32 v25, v29, v17
	v_mul_f32_e32 v22, v28, v18
	v_mul_f32_e32 v26, v29, v18
	v_mul_f32_e32 v23, v28, v19
	v_mul_f32_e32 v27, v29, v19
	v_exp_f32_e32 v20, v20
	v_exp_f32_e32 v21, v21
	v_exp_f32_e32 v22, v22
	v_exp_f32_e32 v23, v23
	v_exp_f32_e32 v24, v24
	v_exp_f32_e32 v25, v25
	v_exp_f32_e32 v26, v26
	v_exp_f32_e32 v27, v27
	v_cvt_pk_f16_f32 v62, v20, v21
	v_cvt_pk_f16_f32 v63, v22, v23
	v_cvt_pk_f16_f32 v94, v24, v25
	v_cvt_pk_f16_f32 v95, v26, v27
.Lblk1_done:
.Lblk2:
	s_cmp_eq_u32 s29, 0
	s_cbranch_scc1 .Lblk2_first
	s_waitcnt vmcnt(4)
	s_branch .Lblk2_go

.Lblk2_go:
	v_add_f32_e32 v160, v160, v161
	v_add_f32_e32 v162, v162, v163
	v_add_f32_e32 v164, v164, v165
	v_add_f32_e32 v166, v166, v167
	v_add_f32_e32 v168, v168, v169
	v_add_f32_e32 v170, v170, v171
	v_add_f32_e32 v172, v172, v173
	v_add_f32_e32 v174, v174, v175
	v_add_f32_e32 v160, v160, v162
	v_add_f32_e32 v164, v164, v166
	v_add_f32_e32 v168, v168, v170
	v_add_f32_e32 v172, v172, v174
	v_cndmask_b32_e64 v162, v160, v164, s[30:31]
	v_cndmask_b32_e64 v166, v168, v172, s[30:31]
	v_cndmask_b32_e64 v161, v164, v160, s[30:31]
	v_cndmask_b32_e64 v165, v172, v168, s[30:31]
	v_add_f32_dpp v161, v162, v161 quad_perm:[1,0,3,2] row_mask:0xf bank_mask:0xf bound_ctrl:1
	v_add_f32_dpp v165, v166, v165 quad_perm:[1,0,3,2] row_mask:0xf bank_mask:0xf bound_ctrl:1
	v_cndmask_b32_e64 v167, v161, v165, s[32:33]
	v_cndmask_b32_e64 v163, v165, v161, s[32:33]
	s_nop 1
	v_add_f32_dpp v163, v167, v163 quad_perm:[2,3,0,1] row_mask:0xf bank_mask:0xf bound_ctrl:1
	v_cvt_f16_f32_e32 v163, v163
	ds_write_b16 v14, v163 offset:2176
	s_cmp_eq_u32 s29, 0
	s_cbranch_scc0 .Lblk2_done
	v_add_u32_e32 v6, 0x8000, v6
	global_load_dwordx4 v[160:163], v6, s[12:13] offset:0 nt
	global_load_dwordx4 v[164:167], v6, s[12:13] offset:1024 nt
	global_load_dwordx4 v[168:171], v6, s[12:13] offset:2048 nt
	global_load_dwordx4 v[172:175], v6, s[12:13] offset:3072 nt
	v_mul_f32_e32 v16, v13, v13
	v_add_f32_e32 v17, 0x3f800000, v13
	v_add_f32_e32 v18, 0x40000000, v13
	v_add_f32_e32 v19, 0x40400000, v13
	v_mul_f32_e32 v17, v17, v17
	v_mul_f32_e32 v18, v18, v18
	v_mul_f32_e32 v19, v19, v19
	v_mul_f32_e32 v20, v8, v16
	v_mul_f32_e32 v24, v9, v16
	v_mul_f32_e32 v21, v8, v17
	v_mul_f32_e32 v25, v9, v17
	v_mul_f32_e32 v22, v8, v18
	v_mul_f32_e32 v26, v9, v18
	v_mul_f32_e32 v23, v8, v19
	v_mul_f32_e32 v27, v9, v19
	v_exp_f32_e32 v20, v20
	v_exp_f32_e32 v21, v21
	v_exp_f32_e32 v22, v22
	v_exp_f32_e32 v23, v23
	v_exp_f32_e32 v24, v24
	v_exp_f32_e32 v25, v25
	v_exp_f32_e32 v26, v26
	v_exp_f32_e32 v27, v27
	v_mul_f32_e32 v96, v10, v20
	v_mul_f32_e32 v97, v10, v21
	v_mul_f32_e32 v98, v10, v22
	v_mul_f32_e32 v99, v10, v23
	v_mul_f32_e32 v112, v11, v24
	v_mul_f32_e32 v113, v11, v25
	v_mul_f32_e32 v114, v11, v26
	v_mul_f32_e32 v115, v11, v27
	v_add_f32_e32 v16, 0x41800000, v13
	v_add_f32_e32 v17, 0x41880000, v13
	v_add_f32_e32 v18, 0x41900000, v13
	v_add_f32_e32 v19, 0x41980000, v13
	v_mul_f32_e32 v16, v16, v16
	v_mul_f32_e32 v17, v17, v17
	v_mul_f32_e32 v18, v18, v18
	v_mul_f32_e32 v19, v19, v19
	v_mul_f32_e32 v20, v8, v16
	v_mul_f32_e32 v24, v9, v16
	v_mul_f32_e32 v21, v8, v17
	v_mul_f32_e32 v25, v9, v17
	v_mul_f32_e32 v22, v8, v18
	v_mul_f32_e32 v26, v9, v18
	v_mul_f32_e32 v23, v8, v19
	v_mul_f32_e32 v27, v9, v19
	v_exp_f32_e32 v20, v20
	v_exp_f32_e32 v21, v21
	v_exp_f32_e32 v22, v22
	v_exp_f32_e32 v23, v23
	v_exp_f32_e32 v24, v24
	v_exp_f32_e32 v25, v25
	v_exp_f32_e32 v26, v26
	v_exp_f32_e32 v27, v27
	v_mul_f32_e32 v100, v10, v20
	v_mul_f32_e32 v101, v10, v21
	v_mul_f32_e32 v102, v10, v22
	v_mul_f32_e32 v103, v10, v23
	v_mul_f32_e32 v116, v11, v24
	v_mul_f32_e32 v117, v11, v25
	v_mul_f32_e32 v118, v11, v26
	v_mul_f32_e32 v119, v11, v27
.Lblk2_done:
.Lblk3:
	s_cmp_eq_u32 s29, 0
	s_cbranch_scc1 .Lblk3_first
	s_waitcnt vmcnt(0)
	s_branch .Lblk3_go

.Lblk3_go:
	v_add_f32_e32 v176, v176, v177
	v_add_f32_e32 v178, v178, v179
	v_add_f32_e32 v180, v180, v181
	v_add_f32_e32 v182, v182, v183
	v_add_f32_e32 v184, v184, v185
	v_add_f32_e32 v186, v186, v187
	v_add_f32_e32 v188, v188, v189
	v_add_f32_e32 v190, v190, v191
	v_add_f32_e32 v176, v176, v178
	v_add_f32_e32 v180, v180, v182
	v_add_f32_e32 v184, v184, v186
	v_add_f32_e32 v188, v188, v190
	v_cndmask_b32_e64 v178, v176, v180, s[30:31]
	v_cndmask_b32_e64 v182, v184, v188, s[30:31]
	v_cndmask_b32_e64 v177, v180, v176, s[30:31]
	v_cndmask_b32_e64 v181, v188, v184, s[30:31]
	v_add_f32_dpp v177, v178, v177 quad_perm:[1,0,3,2] row_mask:0xf bank_mask:0xf bound_ctrl:1
	v_add_f32_dpp v181, v182, v181 quad_perm:[1,0,3,2] row_mask:0xf bank_mask:0xf bound_ctrl:1
	v_cndmask_b32_e64 v183, v177, v181, s[32:33]
	v_cndmask_b32_e64 v179, v181, v177, s[32:33]
	s_nop 1
	v_add_f32_dpp v179, v183, v179 quad_perm:[2,3,0,1] row_mask:0xf bank_mask:0xf bound_ctrl:1
	v_cvt_f16_f32_e32 v179, v179
	ds_write_b16 v14, v179 offset:3264
	s_cmp_eq_u32 s29, 0
	s_cbranch_scc0 .Lblk3_done
	v_add_u32_e32 v6, 0x8000, v6
	global_load_dwordx4 v[176:179], v6, s[12:13] offset:0 nt
	global_load_dwordx4 v[180:183], v6, s[12:13] offset:1024 nt
	global_load_dwordx4 v[184:187], v6, s[12:13] offset:2048 nt
	global_load_dwordx4 v[188:191], v6, s[12:13] offset:3072 nt
	v_mul_f32_e32 v16, v3, v3
	v_add_f32_e32 v17, 0x3f800000, v3
	v_add_f32_e32 v18, 0x40000000, v3
	v_add_f32_e32 v19, 0x40400000, v3
	v_mul_f32_e32 v17, v17, v17
	v_mul_f32_e32 v18, v18, v18
	v_mul_f32_e32 v19, v19, v19
	v_mul_f32_e32 v20, v28, v16
	v_mul_f32_e32 v24, v29, v16
	v_mul_f32_e32 v21, v28, v17
	v_mul_f32_e32 v25, v29, v17
	v_mul_f32_e32 v22, v28, v18
	v_mul_f32_e32 v26, v29, v18
	v_mul_f32_e32 v23, v28, v19
	v_mul_f32_e32 v27, v29, v19
	v_exp_f32_e32 v20, v20
	v_exp_f32_e32 v21, v21
	v_exp_f32_e32 v22, v22
	v_exp_f32_e32 v23, v23
	v_exp_f32_e32 v24, v24
	v_exp_f32_e32 v25, v25
	v_exp_f32_e32 v26, v26
	v_exp_f32_e32 v27, v27
	v_mul_f32_e32 v104, v30, v20
	v_mul_f32_e32 v105, v30, v21
	v_mul_f32_e32 v106, v30, v22
	v_mul_f32_e32 v107, v30, v23
	v_mul_f32_e32 v120, v31, v24
	v_mul_f32_e32 v121, v31, v25
	v_mul_f32_e32 v122, v31, v26
	v_mul_f32_e32 v123, v31, v27
	v_add_f32_e32 v16, 0x41800000, v3
	v_add_f32_e32 v17, 0x41880000, v3
	v_add_f32_e32 v18, 0x41900000, v3
	v_add_f32_e32 v19, 0x41980000, v3
	v_mul_f32_e32 v16, v16, v16
	v_mul_f32_e32 v17, v17, v17
	v_mul_f32_e32 v18, v18, v18
	v_mul_f32_e32 v19, v19, v19
	v_mul_f32_e32 v20, v28, v16
	v_mul_f32_e32 v24, v29, v16
	v_mul_f32_e32 v21, v28, v17
	v_mul_f32_e32 v25, v29, v17
	v_mul_f32_e32 v22, v28, v18
	v_mul_f32_e32 v26, v29, v18
	v_mul_f32_e32 v23, v28, v19
	v_mul_f32_e32 v27, v29, v19
	v_exp_f32_e32 v20, v20
	v_exp_f32_e32 v21, v21
	v_exp_f32_e32 v22, v22
	v_exp_f32_e32 v23, v23
	v_exp_f32_e32 v24, v24
	v_exp_f32_e32 v25, v25
	v_exp_f32_e32 v26, v26
	v_exp_f32_e32 v27, v27
	v_mul_f32_e32 v108, v30, v20
	v_mul_f32_e32 v109, v30, v21
	v_mul_f32_e32 v110, v30, v22
	v_mul_f32_e32 v111, v30, v23
	v_mul_f32_e32 v124, v31, v24
	v_mul_f32_e32 v125, v31, v25
	v_mul_f32_e32 v126, v31, v26
	v_mul_f32_e32 v127, v31, v27
.Lblk3_done:
.Lpass:
	s_waitcnt lgkmcnt(0)
	s_barrier
	ds_read_b128 v[208:211], v15 offset:0
	ds_read_b128 v[212:215], v15 offset:64
	ds_read_b128 v[216:219], v15 offset:128
	ds_read_b128 v[220:223], v15 offset:192
	s_waitcnt lgkmcnt(3)
	v_mfma_f32_16x16x32_f16 v[192:195], v[208:211], v[32:35], 0
	v_mfma_f32_16x16x32_f16 v[200:203], v[208:211], v[64:67], 0
	v_mfma_f32_16x16x32_f16 v[196:199], v[208:211], v[48:51], 0
	v_mfma_f32_16x16x32_f16 v[204:207], v[208:211], v[80:83], 0
	s_waitcnt lgkmcnt(2)
	v_mfma_f32_16x16x32_f16 v[192:195], v[212:215], v[36:39], v[192:195]
	v_mfma_f32_16x16x32_f16 v[200:203], v[212:215], v[68:71], v[200:203]
	v_mfma_f32_16x16x32_f16 v[196:199], v[212:215], v[52:55], v[196:199]
	v_mfma_f32_16x16x32_f16 v[204:207], v[212:215], v[84:87], v[204:207]
	s_waitcnt lgkmcnt(1)
	v_mfma_f32_16x16x32_f16 v[192:195], v[216:219], v[40:43], v[192:195]
	v_mfma_f32_16x16x32_f16 v[200:203], v[216:219], v[72:75], v[200:203]
	v_mfma_f32_16x16x32_f16 v[196:199], v[216:219], v[56:59], v[196:199]
	v_mfma_f32_16x16x32_f16 v[204:207], v[216:219], v[88:91], v[204:207]
	s_waitcnt lgkmcnt(0)
	v_mfma_f32_16x16x32_f16 v[192:195], v[220:223], v[44:47], v[192:195]
	v_mfma_f32_16x16x32_f16 v[200:203], v[220:223], v[76:79], v[200:203]
	v_mfma_f32_16x16x32_f16 v[196:199], v[220:223], v[60:63], v[196:199]
	v_mfma_f32_16x16x32_f16 v[204:207], v[220:223], v[92:95], v[204:207]
	s_nop 15
	v_fma_f32 v224, v96, v192, v224
	v_fma_f32 v225, -v112, v200, v225
	v_fma_f32 v226, v104, v196, v226
	v_fma_f32 v227, -v120, v204, v227
	v_fma_f32 v224, v97, v193, v224
	v_fma_f32 v225, -v113, v201, v225
	v_fma_f32 v226, v105, v197, v226
	v_fma_f32 v227, -v121, v205, v227
	v_fma_f32 v224, v98, v194, v224
	v_fma_f32 v225, -v114, v202, v225
	v_fma_f32 v226, v106, v198, v226
	v_fma_f32 v227, -v122, v206, v227
	v_fma_f32 v224, v99, v195, v224
	v_fma_f32 v225, -v115, v203, v225
	v_fma_f32 v226, v107, v199, v226
	v_fma_f32 v227, -v123, v207, v227
	v_add_f32_e32 v228, v224, v225
	v_add_f32_e32 v229, v226, v227
	v_cmp_gt_u32_e32 vcc, 32, v1
	s_cmp_eq_u32 s29, 1
	v_permlane16_swap_b32_e32 v228, v229
	s_nop 0
	v_add_f32_e32 v228, v228, v229
	v_mov_b32_e32 v229, v228
	s_nop 1
	v_permlane32_swap_b32_e32 v228, v229
	s_nop 0
	v_add_f32_e32 v228, v228, v229
	s_cbranch_scc1 .Lstore
	s_mov_b32 s29, 1
	v_add_u32_e32 v14, 0x1100, v14
	v_add_u32_e32 v15, 0x1100, v15
	v_mov_b32_e32 v96, v100
	v_mov_b32_e32 v112, v116
	v_mov_b32_e32 v97, v101
	v_mov_b32_e32 v113, v117
	v_mov_b32_e32 v98, v102
	v_mov_b32_e32 v114, v118
	v_mov_b32_e32 v99, v103
	v_mov_b32_e32 v115, v119
	v_mov_b32_e32 v104, v108
	v_mov_b32_e32 v120, v124
	v_mov_b32_e32 v105, v109
	v_mov_b32_e32 v121, v125
	v_mov_b32_e32 v106, v110
	v_mov_b32_e32 v122, v126
	v_mov_b32_e32 v107, v111
	v_mov_b32_e32 v123, v127
	s_branch .Lblk0
.Lstore:
	s_and_saveexec_b64 s[2:3], vcc
	s_cbranch_execz .Ldog_main_done
	global_store_dword v5, v228, s[26:27]
